# layers 0-2: workgroups with no tile in the last out-projection step run norm2 for the first third of the rows meanwhile; the norm2 phase proper covers the rest (96 rows per workgroup)
# baseline (speedup 1.0000x reference)
.LBB0_852:
	s_or_b64 exec, exec, s[4:5]
	v_readlane_b32 s6, v254, 24
	v_readlane_b32 s7, v254, 25
	s_mov_b64 s[4:5], -1
	s_and_b64 vcc, exec, s[6:7]
	s_waitcnt lgkmcnt(0)
	s_barrier
	s_mov_b32 s100, 0
	s_cbranch_vccz .LBB0_1086
	s_mov_b64 s[6:7], s[96:97]
	s_lshl_b64 s[4:5], s[44:45], 21
	v_readlane_b32 s1, v254, 0
	s_mov_b32 s2, s80
	v_mov_b32_e32 v16, v0
	s_cmpk_gt_i32 s2, 0x1ff
	v_readfirstlane_b32 s22, v16
	s_cbranch_scc1 .LBB0_875
	s_ashr_i32 s8, s2, 31
	s_lshr_b32 s8, s8, 29
	s_add_i32 s12, s2, s8
	s_and_b32 s8, s12, -8
	s_sub_i32 s10, s2, s8
	s_cmp_gt_i32 s10, -1
	s_mov_b64 s[8:9], -1
	s_cbranch_scc0 .LBB0_856
	s_lshl_b32 s11, s10, 6
	s_mov_b64 s[8:9], 0

.LBB0_1033:
	v_readlane_b32 s1, v254, 7
	s_nop 0
	s_cmp_lt_u32 s1, 0x80
	s_cbranch_scc1 .Lmy_n2_ret
	s_mov_b32 s100, 1
	s_branch .LBB0_1234
.Lmy_n2_ret:
	s_mov_b32 s100, 2
	s_mov_b64 s[6:7], s[96:97]
	s_getreg_b32 s1, hwreg(HW_REG_XCC_ID, 0, 4)
	s_waitcnt vmcnt(0)
	s_waitcnt vmcnt(0) lgkmcnt(0)
	s_barrier
	s_and_saveexec_b64 s[4:5], s[20:21]
	s_cbranch_execz .LBB0_1085
	v_readlane_b32 s2, v254, 22
	s_load_dwordx2 s[6:7], s[6:7], 0xe0
	s_waitcnt vmcnt(0) expcnt(0) lgkmcnt(0)
	v_mov_b32_e32 v2, s2
	ds_read_b32 v4, v2
	v_readlane_b32 s2, v254, 23
	s_and_b32 s1, s1, 15
	s_waitcnt lgkmcnt(0)
	v_cmp_ne_u32_e32 vcc, 0, v4
	v_mov_b32_e32 v2, s2
	ds_read_b32 v2, v2
	s_cbranch_vccnz .LBB0_1049
	v_readlane_b32 s8, v254, 3
	v_readlane_b32 s9, v254, 4
	s_load_dwordx2 s[12:13], s[8:9], 0x4
	s_add_u32 s8, s6, 0x1000
	s_addc_u32 s9, s7, 0
	s_add_u32 s10, s6, 0x1100
	s_addc_u32 s11, s7, 0
	v_readlane_b32 s2, v254, 0
	s_waitcnt lgkmcnt(0)
	s_mul_i32 s2, s12, s2
	s_add_u32 s12, s6, 0x1200
	s_mul_i32 s2, s2, s13
	s_addc_u32 s13, s7, 0
	s_add_u32 s14, s6, 0x1300
	s_addc_u32 s15, s7, 0
	s_mov_b32 s22, 1
	s_branch .LBB0_1037

.LBB0_1237:
	s_or_b64 exec, exec, s[4:5]
	v_readlane_b32 s2, v254, 0
	s_mov_b32 s1, s2
	s_waitcnt lgkmcnt(0)
	s_barrier
	s_abs_i32 s4, s2
	v_cvt_f32_u32_e32 v2, s4
	s_sub_i32 s5, 0, s4
	s_add_i32 s1, s1, 0x8fff
	s_xor_b32 s2, s1, s2
	v_rcp_iflag_f32_e32 v2, v2
	s_abs_i32 s1, s1
	s_ashr_i32 s2, s2, 31
	v_mul_f32_e32 v2, 0x4f7ffffe, v2
	v_cvt_u32_f32_e32 v2, v2
	s_nop 0
	v_readfirstlane_b32 s6, v2
	s_mul_i32 s5, s5, s6
	s_mul_hi_u32 s5, s6, s5
	s_add_i32 s6, s6, s5
	s_mul_hi_u32 s5, s1, s6
	s_mul_i32 s6, s5, s4
	s_sub_i32 s1, s1, s6
	s_add_i32 s6, s5, 1
	s_sub_i32 s7, s1, s4
	s_cmp_ge_u32 s1, s4
	s_cselect_b32 s5, s6, s5
	s_cselect_b32 s1, s7, s1
	s_add_i32 s6, s5, 1
	s_cmp_ge_u32 s1, s4
	s_cselect_b32 s1, s6, s5
	s_xor_b32 s1, s1, s2
	s_sub_i32 s1, s1, s2
	s_add_i32 s1, s1, 1
	s_and_b32 s1, s1, -2
	s_mov_b32 s2, s80
	s_mul_i32 s33, s1, s2
	s_add_i32 s1, s33, s1
	s_min_i32 s1, s1, 0x9000
	s_cmp_eq_u32 s100, 0
	s_cbranch_scc1 .Lmy_n2_rng
	s_cmp_eq_u32 s100, 1
	s_cbranch_scc1 .Lmy_n2_early
	s_mul_i32 s33, s80, 0x60
	s_add_i32 s33, s33, 0x3000
	s_branch .Lmy_n2_set
.Lmy_n2_early:
	s_add_i32 s33, s80, 0xffffff80
	s_mul_i32 s33, s33, 0x60
.Lmy_n2_set:
	s_add_i32 s1, s33, 0x60
.Lmy_n2_rng:
	s_cmp_ge_i32 s33, s1
	s_cbranch_scc1 .LBB0_1265
	v_and_b32_e32 v4, 63, v118
	v_ashrrev_i32_e32 v2, 5, v118
	v_lshlrev_b32_e32 v18, 3, v4
	v_mov_b32_e32 v19, v131
	v_and_b32_e32 v119, -2, v2
	v_lshl_add_u64 v[2:3], s[62:63], 0, v[18:19]
	s_mov_b64 s[6:7], 0x38068000
	v_lshl_add_u64 v[20:21], v[2:3], 0, s[6:7]
	s_mov_b64 s[6:7], 0x5ed68000
	v_lshl_add_u64 v[22:23], v[2:3], 0, s[6:7]
	v_and_b32_e32 v2, 32, v118
	v_cmp_eq_u32_e64 s[6:7], 0, v2
	v_and_b32_e32 v2, 16, v118
	v_cmp_eq_u32_e64 s[8:9], 0, v2
	v_and_b32_e32 v2, 8, v118
	v_cmp_eq_u32_e64 s[10:11], 0, v2
	v_and_b32_e32 v2, 4, v118
	s_add_u32 s64, s62, 0x41068000
	v_cmp_eq_u32_e64 s[12:13], 0, v2
	v_and_b32_e32 v2, 3, v118
	s_addc_u32 s65, s63, 0
	v_lshlrev_b32_e32 v130, 2, v4
	v_cmp_eq_u32_e64 s[14:15], 0, v2
	v_and_b32_e32 v2, 60, v118
	v_mov_b32_e32 v3, v131
	s_add_u32 s2, s62, 0x33810000
	v_lshlrev_b32_e32 v19, 4, v4
	v_mul_u32_u24_e32 v120, 0x50, v4
	v_lshl_add_u64 v[4:5], s[62:63], 0, v[2:3]
	s_mov_b64 s[16:17], 0x70d68000
	v_or_b32_e32 v28, 0x100, v130
	s_addc_u32 s27, s63, 0
	v_lshl_add_u64 v[24:25], v[4:5], 0, s[16:17]
	s_add_i32 s16, 0, 0x15000
	s_add_i32 s17, 0, 0x16000
	v_lshlrev_b32_e32 v3, 2, v28
	v_or_b32_e32 v30, 0x200, v130
	v_add_u32_e32 v123, s16, v3
	v_add_u32_e32 v124, s17, v3
	v_lshlrev_b32_e32 v3, 2, v30
	v_or_b32_e32 v32, 0x300, v130
	s_movk_i32 s4, 0x300
	s_lshl_b32 s22, s44, 10
	v_add_u32_e32 v125, s16, v3
	v_add_u32_e32 v126, s17, v3
	v_lshlrev_b32_e32 v3, 2, v32
	v_cmp_gt_i32_e64 s[4:5], s4, v118
	v_add_u32_e32 v121, s16, v19
	v_add_u32_e32 v122, s17, v19
	v_lshl_add_u64 v[26:27], s[64:65], 0, v[130:131]
	v_mov_b32_e32 v29, v131
	v_mov_b32_e32 v31, v131
	v_add_u32_e32 v127, s16, v3
	v_add_u32_e32 v128, s17, v3
	v_mov_b32_e32 v33, v131
	v_lshlrev_b32_e32 v129, 2, v118
	v_add_u32_e32 v132, 17, v119
	v_or_b32_e32 v34, 0x70d68000, v2
	v_mov_b32_e32 v35, v131
	s_lshl_b64 s[66:67], s[22:23], 2
	s_branch .LBB0_1242

.LBB0_1261:
	s_or_b64 exec, exec, s[16:17]
	v_lshlrev_b32_e32 v109, 16, v102
	v_lshlrev_b32_e32 v108, 16, v106
	v_lshlrev_b32_e32 v111, 16, v100
	v_lshlrev_b32_e32 v110, 16, v104
	s_waitcnt lgkmcnt(3)
	v_pk_fma_f32 v[112:113], v[14:15], v[110:111], v[108:109] op_sel_hi:[0,1,1]
	v_and_b32_e32 v109, 0xffff0000, v102
	v_and_b32_e32 v108, 0xffff0000, v106
	v_and_b32_e32 v111, 0xffff0000, v100
	v_and_b32_e32 v110, 0xffff0000, v104
	v_pk_fma_f32 v[116:117], v[14:15], v[110:111], v[108:109] op_sel:[1,0,0]
	v_lshlrev_b32_e32 v15, 16, v103
	v_lshlrev_b32_e32 v14, 16, v107
	v_lshlrev_b32_e32 v109, 16, v101
	v_lshlrev_b32_e32 v108, 16, v105
	v_pk_fma_f32 v[140:141], v[16:17], v[108:109], v[14:15] op_sel_hi:[0,1,1]
	v_and_b32_e32 v15, 0xffff0000, v103
	v_and_b32_e32 v14, 0xffff0000, v107
	v_and_b32_e32 v101, 0xffff0000, v101
	v_and_b32_e32 v100, 0xffff0000, v105
	v_mov_b32_e32 v16, v17
	v_pk_fma_f32 v[16:17], v[16:17], v[100:101], v[14:15] op_sel_hi:[0,1,1]
	v_pk_mul_f32 v[14:15], v[116:117], v[116:117]
	v_lshlrev_b32_e32 v101, 16, v92
	v_pk_fma_f32 v[14:15], v[112:113], v[112:113], v[14:15]
	v_lshlrev_b32_e32 v100, 16, v96
	v_pk_fma_f32 v[14:15], v[140:141], v[140:141], v[14:15]
	s_mov_b32 s16, 0x3a800000
	v_pk_fma_f32 v[104:105], v[16:17], v[16:17], v[14:15]
	v_lshlrev_b32_e32 v15, 16, v94
	v_lshlrev_b32_e32 v14, 16, v98
	s_waitcnt lgkmcnt(2)
	v_pk_fma_f32 v[102:103], v[10:11], v[100:101], v[14:15] op_sel_hi:[0,1,1]
	v_and_b32_e32 v15, 0xffff0000, v94
	v_and_b32_e32 v14, 0xffff0000, v98
	v_and_b32_e32 v101, 0xffff0000, v92
	v_and_b32_e32 v100, 0xffff0000, v96
	v_pk_fma_f32 v[106:107], v[10:11], v[100:101], v[14:15] op_sel:[1,0,0]
	v_lshlrev_b32_e32 v11, 16, v95
	v_lshlrev_b32_e32 v10, 16, v99
	v_lshlrev_b32_e32 v15, 16, v93
	v_lshlrev_b32_e32 v14, 16, v97
	v_pk_fma_f32 v[108:109], v[12:13], v[14:15], v[10:11] op_sel_hi:[0,1,1]
	v_and_b32_e32 v11, 0xffff0000, v95
	v_and_b32_e32 v10, 0xffff0000, v99
	v_and_b32_e32 v15, 0xffff0000, v93
	v_and_b32_e32 v14, 0xffff0000, v97
	v_mov_b32_e32 v12, v13
	v_pk_fma_f32 v[110:111], v[12:13], v[14:15], v[10:11] op_sel_hi:[0,1,1]
	v_pk_mul_f32 v[10:11], v[106:107], v[106:107]
	v_lshlrev_b32_e32 v13, 16, v84
	v_pk_fma_f32 v[10:11], v[102:103], v[102:103], v[10:11]
	v_lshlrev_b32_e32 v12, 16, v88
	v_pk_fma_f32 v[10:11], v[108:109], v[108:109], v[10:11]
	v_and_b32_e32 v15, 0xffff0000, v84
	v_pk_fma_f32 v[94:95], v[110:111], v[110:111], v[10:11]
	v_lshlrev_b32_e32 v11, 16, v86
	v_lshlrev_b32_e32 v10, 16, v90
	s_waitcnt lgkmcnt(1)
	v_pk_fma_f32 v[10:11], v[6:7], v[12:13], v[10:11] op_sel_hi:[0,1,1]
	v_and_b32_e32 v13, 0xffff0000, v86
	v_and_b32_e32 v12, 0xffff0000, v90
	v_and_b32_e32 v14, 0xffff0000, v88
	v_pk_fma_f32 v[12:13], v[6:7], v[14:15], v[12:13] op_sel:[1,0,0]
	v_lshlrev_b32_e32 v7, 16, v87
	v_lshlrev_b32_e32 v6, 16, v91
	v_lshlrev_b32_e32 v15, 16, v85
	v_lshlrev_b32_e32 v14, 16, v89
	v_pk_fma_f32 v[98:99], v[8:9], v[14:15], v[6:7] op_sel_hi:[0,1,1]
	v_pk_mul_f32 v[6:7], v[12:13], v[12:13]
	v_and_b32_e32 v15, 0xffff0000, v85
	v_pk_fma_f32 v[6:7], v[10:11], v[10:11], v[6:7]
	v_and_b32_e32 v14, 0xffff0000, v89
	v_pk_fma_f32 v[96:97], v[98:99], v[98:99], v[6:7]
	v_and_b32_e32 v7, 0xffff0000, v87
	v_and_b32_e32 v6, 0xffff0000, v91
	v_mov_b32_e32 v8, v9
	v_pk_fma_f32 v[100:101], v[8:9], v[14:15], v[6:7] op_sel_hi:[0,1,1]
	v_and_b32_e32 v7, 0xffff0000, v79
	v_and_b32_e32 v6, 0xffff0000, v83
	v_and_b32_e32 v9, 0xffff0000, v77
	v_and_b32_e32 v8, 0xffff0000, v81
	s_waitcnt lgkmcnt(0)
	v_mov_b32_e32 v14, v5
	v_pk_fma_f32 v[6:7], v[14:15], v[8:9], v[6:7] op_sel_hi:[0,1,1]
	v_lshlrev_b32_e32 v9, 16, v78
	v_lshlrev_b32_e32 v8, 16, v82
	v_lshlrev_b32_e32 v15, 16, v76
	v_lshlrev_b32_e32 v14, 16, v80
	v_pk_fma_f32 v[14:15], v[2:3], v[14:15], v[8:9] op_sel_hi:[0,1,1]
	v_and_b32_e32 v9, 0xffff0000, v78
	v_and_b32_e32 v8, 0xffff0000, v82
	v_and_b32_e32 v85, 0xffff0000, v76
	v_and_b32_e32 v84, 0xffff0000, v80
	v_pk_fma_f32 v[90:91], v[2:3], v[84:85], v[8:9] op_sel:[1,0,0]
	v_lshlrev_b32_e32 v9, 16, v79
	v_pk_mul_f32 v[2:3], v[90:91], v[90:91]
	v_lshlrev_b32_e32 v8, 16, v83
	v_lshlrev_b32_e32 v77, 16, v77
	v_lshlrev_b32_e32 v76, 16, v81
	v_pk_fma_f32 v[2:3], v[14:15], v[14:15], v[2:3]
	v_pk_fma_f32 v[92:93], v[4:5], v[76:77], v[8:9] op_sel_hi:[0,1,1]
	v_pk_add_f32 v[4:5], v[104:105], v[94:95]
	v_pk_fma_f32 v[8:9], v[100:101], v[100:101], v[96:97]
	v_pk_fma_f32 v[2:3], v[92:93], v[92:93], v[2:3]
	v_pk_add_f32 v[4:5], v[4:5], v[8:9]
	v_pk_fma_f32 v[2:3], v[6:7], v[6:7], v[2:3]
	s_nop 0
	v_pk_add_f32 v[2:3], v[4:5], v[2:3]
	s_nop 1
	v_add_f32_dpp v2, v2, v2 quad_perm:[1,0,3,2] row_mask:0xf bank_mask:0xf
	v_add_f32_dpp v3, v3, v3 quad_perm:[1,0,3,2] row_mask:0xf bank_mask:0xf
	s_nop 0
	v_add_f32_dpp v2, v2, v2 quad_perm:[2,3,0,1] row_mask:0xf bank_mask:0xf
	v_add_f32_dpp v3, v3, v3 quad_perm:[2,3,0,1] row_mask:0xf bank_mask:0xf
	s_nop 0
	v_add_f32_dpp v2, v2, v2 row_half_mirror row_mask:0xf bank_mask:0xf
	v_add_f32_dpp v3, v3, v3 row_half_mirror row_mask:0xf bank_mask:0xf
	s_nop 0
	v_add_f32_dpp v2, v2, v2 row_mirror row_mask:0xf bank_mask:0xf
	v_add_f32_dpp v3, v3, v3 row_mirror row_mask:0xf bank_mask:0xf
	s_nop 0
	v_add_f32_dpp v2, v2, v2 row_bcast:15 row_mask:0xa bank_mask:0xf
	v_add_f32_dpp v3, v3, v3 row_bcast:15 row_mask:0xa bank_mask:0xf
	s_nop 0
	v_add_f32_dpp v2, v2, v2 row_bcast:31 row_mask:0xc bank_mask:0xf
	v_add_f32_dpp v3, v3, v3 row_bcast:31 row_mask:0xc bank_mask:0xf
	s_nop 0
	v_readlane_b32 vcc_lo, v2, 63
	v_readlane_b32 vcc_hi, v3, 63
	s_nop 1
	v_mov_b32_e32 v2, vcc_lo
	v_mov_b32_e32 v3, vcc_hi
	s_nop 0
	v_pk_fma_f32 v[2:3], v[2:3], s[16:17], v[176:177] op_sel_hi:[1,0,0]
	s_nop 0
	v_mul_f32_e32 v4, 0x4b800000, v3
	v_cmp_gt_f32_e32 vcc, s25, v3
	v_cmp_gt_f32_e64 s[16:17], s25, v2
	s_nop 0
	v_cndmask_b32_e32 v3, v3, v4, vcc
	v_mul_f32_e32 v4, 0x4b800000, v2
	v_rsq_f32_e32 v3, v3
	v_cndmask_b32_e64 v2, v2, v4, s[16:17]
	v_rsq_f32_e32 v2, v2
	v_mul_f32_e32 v4, 0x45800000, v3
	v_cndmask_b32_e32 v4, v3, v4, vcc
	v_mul_f32_e32 v3, 0x45800000, v2
	v_cndmask_b32_e64 v104, v2, v3, s[16:17]
	ds_read_b128 v[76:79], v121
	ds_read_b128 v[86:89], v122
	v_mov_b32_e32 v2, v113
	v_mov_b32_e32 v3, v117
	v_pk_mul_f32 v[2:3], v[2:3], v[4:5] op_sel_hi:[1,0]
	v_mov_b32_e32 v8, v141
	v_mov_b32_e32 v9, v17
	s_waitcnt lgkmcnt(0)
	v_pk_fma_f32 v[94:95], v[76:77], v[2:3], v[86:87]
	v_pk_mul_f32 v[8:9], v[8:9], v[4:5] op_sel_hi:[1,0]
	v_med3_f32 v2, v94, s26, v209
	v_med3_f32 v3, v95, s26, v209
	v_mov_b32_e32 v5, v131
	v_cvt_pk_fp8_f32 v5, v2, v3
	v_pk_fma_f32 v[82:83], v[78:79], v[8:9], v[88:89]
	s_mov_b32 s16, 0x41068000
	v_med3_f32 v2, v82, s26, v209
	v_med3_f32 v3, v83, s26, v209
	v_cvt_pk_fp8_f32 v5, v2, v3 op_sel:[0,0,1]
	v_lshl_add_u64 v[2:3], s[62:63], 0, v[40:41]
	v_add_co_u32_e32 v114, vcc, s16, v2
	v_mov_b32_e32 v113, v116
	s_nop 0
	v_addc_co_u32_e32 v115, vcc, 0, v3, vcc
	v_pk_mul_f32 v[2:3], v[112:113], v[104:105] op_sel_hi:[1,0]
	global_store_dword v[114:115], v5, off
	v_pk_fma_f32 v[96:97], v[76:77], v[2:3], v[86:87]
	v_mov_b32_e32 v5, v131
	v_med3_f32 v2, v96, s26, v209
	v_med3_f32 v3, v97, s26, v209
	v_mov_b32_e32 v141, v16
	v_cvt_pk_fp8_f32 v5, v2, v3
	v_pk_mul_f32 v[8:9], v[140:141], v[104:105] op_sel_hi:[1,0]
	s_nop 0
	v_pk_fma_f32 v[84:85], v[78:79], v[8:9], v[88:89]
	s_nop 0
	v_med3_f32 v2, v84, s26, v209
	v_med3_f32 v3, v85, s26, v209
	v_cvt_pk_fp8_f32 v5, v2, v3 op_sel:[0,0,1]
	v_add_u32_e32 v2, -16, v36
	v_ashrrev_i32_e32 v3, 31, v2
	v_lshlrev_b64 v[8:9], 10, v[2:3]
	v_lshl_add_u64 v[16:17], v[26:27], 0, v[8:9]
	global_store_dword v[16:17], v5, off
	ds_read_b128 v[78:81], v123
	ds_read_b128 v[140:143], v124
	v_mov_b32_e32 v16, v103
	v_mov_b32_e32 v17, v107
	v_pk_mul_f32 v[76:77], v[16:17], v[4:5] op_sel_hi:[1,0]
	v_mov_b32_e32 v16, v109
	v_mov_b32_e32 v17, v111
	s_waitcnt lgkmcnt(0)
	v_pk_fma_f32 v[86:87], v[76:77], v[78:79], v[140:141]
	v_pk_mul_f32 v[16:17], v[16:17], v[4:5] op_sel_hi:[1,0]
	v_med3_f32 v5, v86, s26, v209
	v_med3_f32 v37, v87, s26, v209
	v_mov_b32_e32 v76, v131
	v_cvt_pk_fp8_f32 v76, v5, v37
	v_pk_fma_f32 v[16:17], v[16:17], v[80:81], v[142:143]
	v_mov_b32_e32 v103, v106
	v_med3_f32 v5, v16, s26, v209
	v_med3_f32 v37, v17, s26, v209
	v_cvt_pk_fp8_f32 v76, v5, v37 op_sel:[0,0,1]
	v_pk_mul_f32 v[88:89], v[102:103], v[104:105] op_sel_hi:[1,0]
	v_mov_b32_e32 v109, v110
	v_pk_fma_f32 v[88:89], v[88:89], v[78:79], v[140:141]
	v_mov_b32_e32 v78, v131
	v_med3_f32 v5, v88, s26, v209
	v_med3_f32 v37, v89, s26, v209
	v_cvt_pk_fp8_f32 v78, v5, v37
	global_store_dword v[114:115], v76, off offset:256
	v_pk_mul_f32 v[76:77], v[108:109], v[104:105] op_sel_hi:[1,0]
	v_lshl_add_u64 v[102:103], s[64:65], 0, v[8:9]
	v_pk_fma_f32 v[76:77], v[76:77], v[80:81], v[142:143]
	v_lshl_add_u64 v[8:9], v[102:103], 0, v[28:29]
	v_med3_f32 v5, v76, s26, v209
	v_med3_f32 v37, v77, s26, v209
	v_cvt_pk_fp8_f32 v78, v5, v37 op_sel:[0,0,1]
	v_mov_b32_e32 v37, v131
	global_store_dword v[8:9], v78, off
	ds_read_b128 v[106:109], v125
	ds_read_b128 v[110:113], v126
	v_mov_b32_e32 v8, v11
	v_mov_b32_e32 v9, v13
	v_pk_mul_f32 v[78:79], v[8:9], v[4:5] op_sel_hi:[1,0]
	v_mov_b32_e32 v8, v99
	v_mov_b32_e32 v9, v101
	s_waitcnt lgkmcnt(0)
	v_pk_fma_f32 v[78:79], v[78:79], v[106:107], v[110:111]
	v_pk_mul_f32 v[8:9], v[8:9], v[4:5] op_sel_hi:[1,0]
	v_med3_f32 v5, v78, s26, v209
	v_med3_f32 v11, v79, s26, v209
	v_mov_b32_e32 v13, v131
	v_cvt_pk_fp8_f32 v13, v5, v11
	v_pk_fma_f32 v[8:9], v[8:9], v[108:109], v[112:113]
	v_mov_b32_e32 v99, v100
	v_med3_f32 v5, v8, s26, v209
	v_med3_f32 v11, v9, s26, v209
	v_cvt_pk_fp8_f32 v13, v5, v11 op_sel:[0,0,1]
	v_mov_b32_e32 v11, v12
	v_pk_mul_f32 v[10:11], v[10:11], v[104:105] op_sel_hi:[1,0]
	global_store_dword v[114:115], v13, off offset:512
	v_pk_fma_f32 v[80:81], v[10:11], v[106:107], v[110:111]
	v_pk_mul_f32 v[12:13], v[98:99], v[104:105] op_sel_hi:[1,0]
	v_med3_f32 v5, v80, s26, v209
	v_med3_f32 v10, v81, s26, v209
	v_cvt_pk_fp8_f32 v37, v5, v10
	v_pk_fma_f32 v[12:13], v[12:13], v[108:109], v[112:113]
	v_mov_b32_e32 v111, v7
	v_med3_f32 v5, v12, s26, v209
	v_med3_f32 v10, v13, s26, v209
	v_cvt_pk_fp8_f32 v37, v5, v10 op_sel:[0,0,1]
	v_lshl_add_u64 v[10:11], v[102:103], 0, v[30:31]
	v_mov_b32_e32 v110, v93
	v_mov_b32_e32 v93, v6
	global_store_dword v[10:11], v37, off
	ds_read_b128 v[98:101], v127
	ds_read_b128 v[106:109], v128
	v_mov_b32_e32 v10, v15
	v_mov_b32_e32 v11, v91
	v_pk_mul_f32 v[10:11], v[10:11], v[4:5] op_sel_hi:[1,0]
	v_mov_b32_e32 v37, v131
	s_waitcnt lgkmcnt(0)
	v_pk_fma_f32 v[10:11], v[10:11], v[98:99], v[106:107]
	v_pk_mul_f32 v[4:5], v[110:111], v[4:5] op_sel_hi:[1,0]
	v_med3_f32 v7, v10, s26, v209
	v_med3_f32 v15, v11, s26, v209
	v_cvt_pk_fp8_f32 v37, v7, v15
	v_pk_fma_f32 v[4:5], v[4:5], v[100:101], v[108:109]
	s_nop 0
	v_med3_f32 v7, v4, s26, v209
	v_med3_f32 v15, v5, s26, v209
	v_cvt_pk_fp8_f32 v37, v7, v15 op_sel:[0,0,1]
	v_mov_b32_e32 v15, v90
	v_pk_mul_f32 v[14:15], v[14:15], v[104:105] op_sel_hi:[1,0]
	v_pk_mul_f32 v[6:7], v[92:93], v[104:105] op_sel_hi:[1,0]
	v_pk_fma_f32 v[14:15], v[14:15], v[98:99], v[106:107]
	global_store_dword v[114:115], v37, off offset:768
	v_med3_f32 v37, v14, s26, v209
	v_med3_f32 v90, v15, s26, v209
	v_mov_b32_e32 v92, v131
	v_cvt_pk_fp8_f32 v92, v37, v90
	v_pk_fma_f32 v[6:7], v[6:7], v[100:101], v[108:109]
	s_nop 0
	v_med3_f32 v37, v6, s26, v209
	v_med3_f32 v90, v7, s26, v209
	v_cvt_pk_fp8_f32 v92, v37, v90 op_sel:[0,0,1]
	v_lshl_add_u64 v[90:91], v[102:103], 0, v[32:33]
	global_store_dword v[90:91], v92, off
	v_mov_b32_e32 v37, v120
	v_mov_b32_e32 v110, v94
	v_add_u32_e32 v37, 0, v37
	ds_read_b128 v[90:93], v37
	ds_read_b128 v[98:101], v37 offset:16
	ds_read_b128 v[102:105], v37 offset:32
	ds_read_b128 v[106:109], v37 offset:48
	v_mov_b32_e32 v111, v96
	s_waitcnt lgkmcnt(3)
	v_pk_fma_f32 v[112:113], v[110:111], v[90:91], 0 op_sel_hi:[1,0,0]
	v_pk_fma_f32 v[114:115], v[110:111], v[90:91], 0 op_sel:[0,1,0] op_sel_hi:[1,1,0]
	v_mov_b32_e32 v90, v93
	v_pk_fma_f32 v[140:141], v[110:111], v[90:91], 0 op_sel_hi:[1,0,0]
	s_waitcnt lgkmcnt(2)
	v_mov_b32_e32 v90, v101
	v_pk_fma_f32 v[148:149], v[110:111], v[90:91], 0 op_sel_hi:[1,0,0]
	s_waitcnt lgkmcnt(1)
	v_mov_b32_e32 v90, v105
	v_pk_fma_f32 v[156:157], v[110:111], v[90:91], 0 op_sel_hi:[1,0,0]
	s_waitcnt lgkmcnt(0)
	v_mov_b32_e32 v90, v109
	v_pk_fma_f32 v[116:117], v[110:111], v[92:93], 0 op_sel_hi:[1,0,0]
	v_pk_fma_f32 v[142:143], v[110:111], v[98:99], 0 op_sel_hi:[1,0,0]
	v_pk_fma_f32 v[144:145], v[110:111], v[98:99], 0 op_sel:[0,1,0] op_sel_hi:[1,1,0]
	v_pk_fma_f32 v[146:147], v[110:111], v[100:101], 0 op_sel_hi:[1,0,0]
	v_pk_fma_f32 v[150:151], v[110:111], v[102:103], 0 op_sel_hi:[1,0,0]
	v_pk_fma_f32 v[152:153], v[110:111], v[102:103], 0 op_sel:[0,1,0] op_sel_hi:[1,1,0]
	v_pk_fma_f32 v[154:155], v[110:111], v[104:105], 0 op_sel_hi:[1,0,0]
	v_pk_fma_f32 v[158:159], v[110:111], v[106:107], 0 op_sel_hi:[1,0,0]
	v_pk_fma_f32 v[160:161], v[110:111], v[106:107], 0 op_sel:[0,1,0] op_sel_hi:[1,1,0]
	v_pk_fma_f32 v[162:163], v[110:111], v[108:109], 0 op_sel_hi:[1,0,0]
	v_pk_fma_f32 v[110:111], v[110:111], v[90:91], 0 op_sel_hi:[1,0,0]
	ds_read_b128 v[90:93], v37 offset:20480
	ds_read_b128 v[98:101], v37 offset:20496
	ds_read_b128 v[102:105], v37 offset:20512
	ds_read_b128 v[106:109], v37 offset:20528
	v_mov_b32_e32 v96, v95
	s_waitcnt lgkmcnt(3)
	v_pk_fma_f32 v[112:113], v[96:97], v[90:91], v[112:113] op_sel_hi:[1,0,1]
	v_pk_fma_f32 v[114:115], v[96:97], v[90:91], v[114:115] op_sel:[0,1,0]
	v_mov_b32_e32 v90, v93
	v_pk_fma_f32 v[140:141], v[96:97], v[90:91], v[140:141] op_sel_hi:[1,0,1]
	s_waitcnt lgkmcnt(2)
	v_mov_b32_e32 v90, v101
	v_pk_fma_f32 v[148:149], v[96:97], v[90:91], v[148:149] op_sel_hi:[1,0,1]
	s_waitcnt lgkmcnt(1)
	v_mov_b32_e32 v90, v105
	v_pk_fma_f32 v[156:157], v[96:97], v[90:91], v[156:157] op_sel_hi:[1,0,1]
	s_waitcnt lgkmcnt(0)
	v_mov_b32_e32 v90, v109
	v_pk_fma_f32 v[116:117], v[96:97], v[92:93], v[116:117] op_sel_hi:[1,0,1]
	v_pk_fma_f32 v[142:143], v[96:97], v[98:99], v[142:143] op_sel_hi:[1,0,1]
	v_pk_fma_f32 v[144:145], v[96:97], v[98:99], v[144:145] op_sel:[0,1,0]
	v_pk_fma_f32 v[146:147], v[96:97], v[100:101], v[146:147] op_sel_hi:[1,0,1]
	v_pk_fma_f32 v[150:151], v[96:97], v[102:103], v[150:151] op_sel_hi:[1,0,1]
	v_pk_fma_f32 v[152:153], v[96:97], v[102:103], v[152:153] op_sel:[0,1,0]
	v_pk_fma_f32 v[154:155], v[96:97], v[104:105], v[154:155] op_sel_hi:[1,0,1]
	v_pk_fma_f32 v[158:159], v[96:97], v[106:107], v[158:159] op_sel_hi:[1,0,1]
	v_pk_fma_f32 v[106:107], v[96:97], v[106:107], v[160:161] op_sel:[0,1,0]
	v_pk_fma_f32 v[160:161], v[96:97], v[108:109], v[162:163] op_sel_hi:[1,0,1]
	v_pk_fma_f32 v[108:109], v[96:97], v[90:91], v[110:111] op_sel_hi:[1,0,1]
	ds_read_b128 v[90:93], v37 offset:40960
	ds_read_b128 v[94:97], v37 offset:40976
	ds_read_b128 v[98:101], v37 offset:40992
	ds_read_b128 v[102:105], v37 offset:41008
	v_mov_b32_e32 v110, v82
	v_mov_b32_e32 v111, v84
	s_waitcnt lgkmcnt(3)
	v_mov_b32_e32 v82, v93
	v_pk_fma_f32 v[140:141], v[110:111], v[82:83], v[140:141] op_sel_hi:[1,0,1]
	s_waitcnt lgkmcnt(2)
	v_mov_b32_e32 v82, v97
	v_pk_fma_f32 v[148:149], v[110:111], v[82:83], v[148:149] op_sel_hi:[1,0,1]
	s_waitcnt lgkmcnt(1)
	v_mov_b32_e32 v82, v101
	v_pk_fma_f32 v[156:157], v[110:111], v[82:83], v[156:157] op_sel_hi:[1,0,1]
	s_waitcnt lgkmcnt(0)
	v_mov_b32_e32 v82, v105
	v_pk_fma_f32 v[112:113], v[110:111], v[90:91], v[112:113] op_sel_hi:[1,0,1]
	v_pk_fma_f32 v[114:115], v[110:111], v[90:91], v[114:115] op_sel:[0,1,0]
	v_pk_fma_f32 v[116:117], v[110:111], v[92:93], v[116:117] op_sel_hi:[1,0,1]
	v_pk_fma_f32 v[142:143], v[110:111], v[94:95], v[142:143] op_sel_hi:[1,0,1]
	v_pk_fma_f32 v[144:145], v[110:111], v[94:95], v[144:145] op_sel:[0,1,0]
	v_pk_fma_f32 v[146:147], v[110:111], v[96:97], v[146:147] op_sel_hi:[1,0,1]
	v_pk_fma_f32 v[150:151], v[110:111], v[98:99], v[150:151] op_sel_hi:[1,0,1]
	v_pk_fma_f32 v[152:153], v[110:111], v[98:99], v[152:153] op_sel:[0,1,0]
	v_pk_fma_f32 v[154:155], v[110:111], v[100:101], v[154:155] op_sel_hi:[1,0,1]
	v_pk_fma_f32 v[158:159], v[110:111], v[102:103], v[158:159] op_sel_hi:[1,0,1]
	v_pk_fma_f32 v[106:107], v[110:111], v[102:103], v[106:107] op_sel:[0,1,0]
	v_pk_fma_f32 v[160:161], v[110:111], v[104:105], v[160:161] op_sel_hi:[1,0,1]
	v_pk_fma_f32 v[108:109], v[110:111], v[82:83], v[108:109] op_sel_hi:[1,0,1]
	ds_read_b128 v[90:93], v37 offset:61440
	ds_read_b128 v[94:97], v37 offset:61456
	ds_read_b128 v[98:101], v37 offset:61472
	ds_read_b128 v[102:105], v37 offset:61488
	v_mov_b32_e32 v84, v83
	s_waitcnt lgkmcnt(3)
	v_mov_b32_e32 v82, v93
	v_pk_fma_f32 v[110:111], v[84:85], v[90:91], v[112:113] op_sel_hi:[1,0,1]
	v_pk_fma_f32 v[112:113], v[84:85], v[90:91], v[114:115] op_sel:[0,1,0]
	v_pk_fma_f32 v[114:115], v[84:85], v[92:93], v[116:117] op_sel_hi:[1,0,1]
	v_pk_fma_f32 v[116:117], v[84:85], v[82:83], v[140:141] op_sel_hi:[1,0,1]
	s_waitcnt lgkmcnt(2)
	v_mov_b32_e32 v82, v97
	v_pk_fma_f32 v[140:141], v[84:85], v[94:95], v[142:143] op_sel_hi:[1,0,1]
	v_pk_fma_f32 v[142:143], v[84:85], v[94:95], v[144:145] op_sel:[0,1,0]
	v_pk_fma_f32 v[144:145], v[84:85], v[96:97], v[146:147] op_sel_hi:[1,0,1]
	v_pk_fma_f32 v[146:147], v[84:85], v[82:83], v[148:149] op_sel_hi:[1,0,1]
	s_waitcnt lgkmcnt(1)
	v_mov_b32_e32 v82, v101
	v_pk_fma_f32 v[148:149], v[84:85], v[98:99], v[150:151] op_sel_hi:[1,0,1]
	v_pk_fma_f32 v[150:151], v[84:85], v[98:99], v[152:153] op_sel:[0,1,0]
	v_pk_fma_f32 v[152:153], v[84:85], v[100:101], v[154:155] op_sel_hi:[1,0,1]
	v_pk_fma_f32 v[154:155], v[84:85], v[82:83], v[156:157] op_sel_hi:[1,0,1]
	s_waitcnt lgkmcnt(0)
	v_mov_b32_e32 v82, v105
	v_pk_fma_f32 v[156:157], v[84:85], v[102:103], v[158:159] op_sel_hi:[1,0,1]
	v_pk_fma_f32 v[102:103], v[84:85], v[102:103], v[106:107] op_sel:[0,1,0]
	v_pk_fma_f32 v[106:107], v[84:85], v[104:105], v[160:161] op_sel_hi:[1,0,1]
	v_pk_fma_f32 v[104:105], v[84:85], v[82:83], v[108:109] op_sel_hi:[1,0,1]
	ds_read_b128 v[82:85], v37 offset:5120
	ds_read_b128 v[90:93], v37 offset:5136
	ds_read_b128 v[94:97], v37 offset:5152
	ds_read_b128 v[98:101], v37 offset:5168
	v_mov_b32_e32 v108, v86
	v_mov_b32_e32 v109, v88
	s_waitcnt lgkmcnt(3)
	v_pk_fma_f32 v[110:111], v[108:109], v[82:83], v[110:111] op_sel_hi:[1,0,1]
	v_pk_fma_f32 v[112:113], v[108:109], v[82:83], v[112:113] op_sel:[0,1,0]
	v_mov_b32_e32 v82, v85
	v_pk_fma_f32 v[116:117], v[108:109], v[82:83], v[116:117] op_sel_hi:[1,0,1]
	s_waitcnt lgkmcnt(2)
	v_mov_b32_e32 v82, v93
	v_pk_fma_f32 v[146:147], v[108:109], v[82:83], v[146:147] op_sel_hi:[1,0,1]
	s_waitcnt lgkmcnt(1)
	v_mov_b32_e32 v82, v97
	v_pk_fma_f32 v[154:155], v[108:109], v[82:83], v[154:155] op_sel_hi:[1,0,1]
	s_waitcnt lgkmcnt(0)
	v_mov_b32_e32 v82, v101
	v_pk_fma_f32 v[114:115], v[108:109], v[84:85], v[114:115] op_sel_hi:[1,0,1]
	v_pk_fma_f32 v[140:141], v[108:109], v[90:91], v[140:141] op_sel_hi:[1,0,1]
	v_pk_fma_f32 v[142:143], v[108:109], v[90:91], v[142:143] op_sel:[0,1,0]
	v_pk_fma_f32 v[144:145], v[108:109], v[92:93], v[144:145] op_sel_hi:[1,0,1]
	v_pk_fma_f32 v[148:149], v[108:109], v[94:95], v[148:149] op_sel_hi:[1,0,1]
	v_pk_fma_f32 v[150:151], v[108:109], v[94:95], v[150:151] op_sel:[0,1,0]
	v_pk_fma_f32 v[152:153], v[108:109], v[96:97], v[152:153] op_sel_hi:[1,0,1]
	v_pk_fma_f32 v[156:157], v[108:109], v[98:99], v[156:157] op_sel_hi:[1,0,1]
	v_pk_fma_f32 v[102:103], v[108:109], v[98:99], v[102:103] op_sel:[0,1,0]
	v_pk_fma_f32 v[106:107], v[108:109], v[100:101], v[106:107] op_sel_hi:[1,0,1]
	v_pk_fma_f32 v[104:105], v[108:109], v[82:83], v[104:105] op_sel_hi:[1,0,1]
	ds_read_b128 v[82:85], v37 offset:25600
	ds_read_b128 v[90:93], v37 offset:25616
	ds_read_b128 v[94:97], v37 offset:25632
	ds_read_b128 v[98:101], v37 offset:25648
	v_mov_b32_e32 v88, v87
	s_waitcnt lgkmcnt(3)
	v_pk_fma_f32 v[108:109], v[88:89], v[82:83], v[110:111] op_sel_hi:[1,0,1]
	v_pk_fma_f32 v[110:111], v[88:89], v[82:83], v[112:113] op_sel:[0,1,0]
	v_mov_b32_e32 v82, v85
	v_pk_fma_f32 v[112:113], v[88:89], v[84:85], v[114:115] op_sel_hi:[1,0,1]
	v_pk_fma_f32 v[114:115], v[88:89], v[82:83], v[116:117] op_sel_hi:[1,0,1]
	s_waitcnt lgkmcnt(2)
	v_mov_b32_e32 v82, v93
	v_pk_fma_f32 v[116:117], v[88:89], v[90:91], v[140:141] op_sel_hi:[1,0,1]
	v_pk_fma_f32 v[140:141], v[88:89], v[90:91], v[142:143] op_sel:[0,1,0]
	v_pk_fma_f32 v[142:143], v[88:89], v[92:93], v[144:145] op_sel_hi:[1,0,1]
	v_pk_fma_f32 v[144:145], v[88:89], v[82:83], v[146:147] op_sel_hi:[1,0,1]
	s_waitcnt lgkmcnt(1)
	v_mov_b32_e32 v82, v97
	v_pk_fma_f32 v[146:147], v[88:89], v[94:95], v[148:149] op_sel_hi:[1,0,1]
	v_pk_fma_f32 v[148:149], v[88:89], v[94:95], v[150:151] op_sel:[0,1,0]
	v_pk_fma_f32 v[150:151], v[88:89], v[96:97], v[152:153] op_sel_hi:[1,0,1]
	v_pk_fma_f32 v[152:153], v[88:89], v[82:83], v[154:155] op_sel_hi:[1,0,1]
	s_waitcnt lgkmcnt(0)
	v_mov_b32_e32 v82, v101
	v_pk_fma_f32 v[154:155], v[88:89], v[98:99], v[156:157] op_sel_hi:[1,0,1]
	v_pk_fma_f32 v[98:99], v[88:89], v[98:99], v[102:103] op_sel:[0,1,0]
	v_pk_fma_f32 v[102:103], v[88:89], v[100:101], v[106:107] op_sel_hi:[1,0,1]
	v_pk_fma_f32 v[100:101], v[88:89], v[82:83], v[104:105] op_sel_hi:[1,0,1]
	ds_read_b128 v[82:85], v37 offset:46080
	ds_read_b128 v[86:89], v37 offset:46096
	ds_read_b128 v[90:93], v37 offset:46112
	ds_read_b128 v[94:97], v37 offset:46128
	v_mov_b32_e32 v104, v16
	v_mov_b32_e32 v105, v76
	s_waitcnt lgkmcnt(3)
	v_mov_b32_e32 v16, v85
	v_pk_fma_f32 v[106:107], v[104:105], v[82:83], v[108:109] op_sel_hi:[1,0,1]
	v_pk_fma_f32 v[108:109], v[104:105], v[82:83], v[110:111] op_sel:[0,1,0]
	v_pk_fma_f32 v[110:111], v[104:105], v[84:85], v[112:113] op_sel_hi:[1,0,1]
	v_pk_fma_f32 v[112:113], v[104:105], v[16:17], v[114:115] op_sel_hi:[1,0,1]
	s_waitcnt lgkmcnt(2)
	v_mov_b32_e32 v16, v89
	v_pk_fma_f32 v[114:115], v[104:105], v[86:87], v[116:117] op_sel_hi:[1,0,1]
	v_pk_fma_f32 v[116:117], v[104:105], v[86:87], v[140:141] op_sel:[0,1,0]
	v_pk_fma_f32 v[140:141], v[104:105], v[88:89], v[142:143] op_sel_hi:[1,0,1]
	v_pk_fma_f32 v[142:143], v[104:105], v[16:17], v[144:145] op_sel_hi:[1,0,1]
	s_waitcnt lgkmcnt(1)
	v_mov_b32_e32 v16, v93
	v_pk_fma_f32 v[144:145], v[104:105], v[90:91], v[146:147] op_sel_hi:[1,0,1]
	v_pk_fma_f32 v[146:147], v[104:105], v[90:91], v[148:149] op_sel:[0,1,0]
	v_pk_fma_f32 v[148:149], v[104:105], v[92:93], v[150:151] op_sel_hi:[1,0,1]
	v_pk_fma_f32 v[150:151], v[104:105], v[16:17], v[152:153] op_sel_hi:[1,0,1]
	s_waitcnt lgkmcnt(0)
	v_mov_b32_e32 v16, v97
	v_pk_fma_f32 v[152:153], v[104:105], v[94:95], v[154:155] op_sel_hi:[1,0,1]
	v_pk_fma_f32 v[98:99], v[104:105], v[94:95], v[98:99] op_sel:[0,1,0]
	v_pk_fma_f32 v[102:103], v[104:105], v[96:97], v[102:103] op_sel_hi:[1,0,1]
	v_pk_fma_f32 v[100:101], v[104:105], v[16:17], v[100:101] op_sel_hi:[1,0,1]
	v_add_u32_e32 v16, 0x10400, v37
	v_add_u32_e32 v76, 0x10410, v37
	ds_read_b128 v[82:85], v16
	ds_read_b128 v[86:89], v76
	v_add_u32_e32 v16, 0x10420, v37
	v_add_u32_e32 v76, 0x10430, v37
	ds_read_b128 v[90:93], v16
	ds_read_b128 v[94:97], v76
	v_mov_b32_e32 v76, v17
	s_waitcnt lgkmcnt(3)
	v_pk_fma_f32 v[16:17], v[76:77], v[82:83], v[106:107] op_sel_hi:[1,0,1]
	v_pk_fma_f32 v[104:105], v[76:77], v[82:83], v[108:109] op_sel:[0,1,0]
	v_mov_b32_e32 v82, v85
	v_pk_fma_f32 v[108:109], v[76:77], v[82:83], v[112:113] op_sel_hi:[1,0,1]
	s_waitcnt lgkmcnt(2)
	v_mov_b32_e32 v82, v89
	v_pk_fma_f32 v[112:113], v[76:77], v[86:87], v[116:117] op_sel:[0,1,0]
	v_pk_fma_f32 v[116:117], v[76:77], v[82:83], v[142:143] op_sel_hi:[1,0,1]
	s_waitcnt lgkmcnt(1)
	v_mov_b32_e32 v82, v93
	v_pk_fma_f32 v[142:143], v[76:77], v[90:91], v[146:147] op_sel:[0,1,0]
	v_pk_fma_f32 v[146:147], v[76:77], v[82:83], v[150:151] op_sel_hi:[1,0,1]
	s_waitcnt lgkmcnt(0)
	v_mov_b32_e32 v82, v97
	v_pk_fma_f32 v[106:107], v[76:77], v[84:85], v[110:111] op_sel_hi:[1,0,1]
	v_pk_fma_f32 v[110:111], v[76:77], v[86:87], v[114:115] op_sel_hi:[1,0,1]
	v_pk_fma_f32 v[114:115], v[76:77], v[88:89], v[140:141] op_sel_hi:[1,0,1]
	v_pk_fma_f32 v[140:141], v[76:77], v[90:91], v[144:145] op_sel_hi:[1,0,1]
	v_pk_fma_f32 v[144:145], v[76:77], v[92:93], v[148:149] op_sel_hi:[1,0,1]
	v_pk_fma_f32 v[148:149], v[76:77], v[94:95], v[152:153] op_sel_hi:[1,0,1]
	v_pk_fma_f32 v[98:99], v[76:77], v[94:95], v[98:99] op_sel:[0,1,0]
	v_pk_fma_f32 v[102:103], v[76:77], v[96:97], v[102:103] op_sel_hi:[1,0,1]
	v_pk_fma_f32 v[76:77], v[76:77], v[82:83], v[100:101] op_sel_hi:[1,0,1]
	ds_read_b128 v[82:85], v37 offset:10240
	ds_read_b128 v[86:89], v37 offset:10256
	ds_read_b128 v[90:93], v37 offset:10272
	ds_read_b128 v[94:97], v37 offset:10288
	v_mov_b32_e32 v100, v78
	v_mov_b32_e32 v101, v80
	s_waitcnt lgkmcnt(3)
	v_mov_b32_e32 v78, v85
	v_pk_fma_f32 v[108:109], v[100:101], v[78:79], v[108:109] op_sel_hi:[1,0,1]
	s_waitcnt lgkmcnt(2)
	v_mov_b32_e32 v78, v89
	v_pk_fma_f32 v[116:117], v[100:101], v[78:79], v[116:117] op_sel_hi:[1,0,1]
	s_waitcnt lgkmcnt(1)
	v_mov_b32_e32 v78, v93
	v_pk_fma_f32 v[146:147], v[100:101], v[78:79], v[146:147] op_sel_hi:[1,0,1]
	s_waitcnt lgkmcnt(0)
	v_mov_b32_e32 v78, v97
	v_pk_fma_f32 v[16:17], v[100:101], v[82:83], v[16:17] op_sel_hi:[1,0,1]
	v_pk_fma_f32 v[76:77], v[100:101], v[78:79], v[76:77] op_sel_hi:[1,0,1]
	v_pk_fma_f32 v[104:105], v[100:101], v[82:83], v[104:105] op_sel:[0,1,0]
	v_pk_fma_f32 v[106:107], v[100:101], v[84:85], v[106:107] op_sel_hi:[1,0,1]
	v_pk_fma_f32 v[110:111], v[100:101], v[86:87], v[110:111] op_sel_hi:[1,0,1]
	v_pk_fma_f32 v[112:113], v[100:101], v[86:87], v[112:113] op_sel:[0,1,0]
	v_pk_fma_f32 v[114:115], v[100:101], v[88:89], v[114:115] op_sel_hi:[1,0,1]
	v_pk_fma_f32 v[140:141], v[100:101], v[90:91], v[140:141] op_sel_hi:[1,0,1]
	v_pk_fma_f32 v[142:143], v[100:101], v[90:91], v[142:143] op_sel:[0,1,0]
	v_pk_fma_f32 v[144:145], v[100:101], v[92:93], v[144:145] op_sel_hi:[1,0,1]
	v_pk_fma_f32 v[148:149], v[100:101], v[94:95], v[148:149] op_sel_hi:[1,0,1]
	v_pk_fma_f32 v[98:99], v[100:101], v[94:95], v[98:99] op_sel:[0,1,0]
	v_pk_fma_f32 v[102:103], v[100:101], v[96:97], v[102:103] op_sel_hi:[1,0,1]
	ds_read_b128 v[82:85], v37 offset:30720
	ds_read_b128 v[86:89], v37 offset:30736
	ds_read_b128 v[90:93], v37 offset:30752
	ds_read_b128 v[94:97], v37 offset:30768
	v_mov_b32_e32 v80, v79
	s_waitcnt lgkmcnt(3)
	v_mov_b32_e32 v78, v85
	v_pk_fma_f32 v[100:101], v[80:81], v[82:83], v[104:105] op_sel:[0,1,0]
	v_pk_fma_f32 v[104:105], v[80:81], v[84:85], v[106:107] op_sel_hi:[1,0,1]
	v_pk_fma_f32 v[106:107], v[80:81], v[78:79], v[108:109] op_sel_hi:[1,0,1]
	s_waitcnt lgkmcnt(2)
	v_mov_b32_e32 v78, v89
	v_pk_fma_f32 v[108:109], v[80:81], v[86:87], v[110:111] op_sel_hi:[1,0,1]
	v_pk_fma_f32 v[110:111], v[80:81], v[86:87], v[112:113] op_sel:[0,1,0]
	v_pk_fma_f32 v[112:113], v[80:81], v[88:89], v[114:115] op_sel_hi:[1,0,1]
	v_pk_fma_f32 v[114:115], v[80:81], v[78:79], v[116:117] op_sel_hi:[1,0,1]
	s_waitcnt lgkmcnt(1)
	v_mov_b32_e32 v78, v93
	v_pk_fma_f32 v[16:17], v[80:81], v[82:83], v[16:17] op_sel_hi:[1,0,1]
	v_pk_fma_f32 v[116:117], v[80:81], v[90:91], v[140:141] op_sel_hi:[1,0,1]
	v_pk_fma_f32 v[140:141], v[80:81], v[90:91], v[142:143] op_sel:[0,1,0]
	v_pk_fma_f32 v[142:143], v[80:81], v[92:93], v[144:145] op_sel_hi:[1,0,1]
	v_pk_fma_f32 v[92:93], v[80:81], v[78:79], v[146:147] op_sel_hi:[1,0,1]
	s_waitcnt lgkmcnt(0)
	v_mov_b32_e32 v78, v97
	v_pk_fma_f32 v[144:145], v[80:81], v[94:95], v[148:149] op_sel_hi:[1,0,1]
	v_pk_fma_f32 v[94:95], v[80:81], v[94:95], v[98:99] op_sel:[0,1,0]
	v_pk_fma_f32 v[98:99], v[80:81], v[96:97], v[102:103] op_sel_hi:[1,0,1]
	v_pk_fma_f32 v[96:97], v[80:81], v[78:79], v[76:77] op_sel_hi:[1,0,1]
	ds_read_b128 v[76:79], v37 offset:51200
	ds_read_b128 v[80:83], v37 offset:51216
	ds_read_b128 v[84:87], v37 offset:51232
	ds_read_b128 v[88:91], v37 offset:51248
	v_mov_b32_e32 v102, v8
	v_mov_b32_e32 v103, v12
	s_waitcnt lgkmcnt(3)
	v_mov_b32_e32 v8, v79
	v_pk_fma_f32 v[106:107], v[102:103], v[8:9], v[106:107] op_sel_hi:[1,0,1]
	s_waitcnt lgkmcnt(2)
	v_mov_b32_e32 v8, v83
	v_pk_fma_f32 v[114:115], v[102:103], v[8:9], v[114:115] op_sel_hi:[1,0,1]
	s_waitcnt lgkmcnt(1)
	v_mov_b32_e32 v8, v87
	v_pk_fma_f32 v[16:17], v[102:103], v[76:77], v[16:17] op_sel_hi:[1,0,1]
	v_pk_fma_f32 v[92:93], v[102:103], v[8:9], v[92:93] op_sel_hi:[1,0,1]
	s_waitcnt lgkmcnt(0)
	v_mov_b32_e32 v8, v91
	v_pk_fma_f32 v[100:101], v[102:103], v[76:77], v[100:101] op_sel:[0,1,0]
	v_pk_fma_f32 v[104:105], v[102:103], v[78:79], v[104:105] op_sel_hi:[1,0,1]
	v_pk_fma_f32 v[108:109], v[102:103], v[80:81], v[108:109] op_sel_hi:[1,0,1]
	v_pk_fma_f32 v[110:111], v[102:103], v[80:81], v[110:111] op_sel:[0,1,0]
	v_pk_fma_f32 v[112:113], v[102:103], v[82:83], v[112:113] op_sel_hi:[1,0,1]
	v_pk_fma_f32 v[116:117], v[102:103], v[84:85], v[116:117] op_sel_hi:[1,0,1]
	v_pk_fma_f32 v[140:141], v[102:103], v[84:85], v[140:141] op_sel:[0,1,0]
	v_pk_fma_f32 v[142:143], v[102:103], v[86:87], v[142:143] op_sel_hi:[1,0,1]
	v_pk_fma_f32 v[144:145], v[102:103], v[88:89], v[144:145] op_sel_hi:[1,0,1]
	v_pk_fma_f32 v[94:95], v[102:103], v[88:89], v[94:95] op_sel:[0,1,0]
	v_pk_fma_f32 v[98:99], v[102:103], v[90:91], v[98:99] op_sel_hi:[1,0,1]
	v_pk_fma_f32 v[96:97], v[102:103], v[8:9], v[96:97] op_sel_hi:[1,0,1]
	v_add_u32_e32 v8, 0x11800, v37
	v_add_u32_e32 v12, 0x11810, v37
	ds_read_b128 v[76:79], v8
	ds_read_b128 v[80:83], v12
	v_add_u32_e32 v8, 0x11820, v37
	v_add_u32_e32 v12, 0x11830, v37
	ds_read_b128 v[84:87], v8
	ds_read_b128 v[88:91], v12
	v_mov_b32_e32 v12, v9
	s_waitcnt lgkmcnt(3)
	v_pk_fma_f32 v[8:9], v[12:13], v[76:77], v[16:17] op_sel_hi:[1,0,1]
	v_pk_fma_f32 v[16:17], v[12:13], v[76:77], v[100:101] op_sel:[0,1,0]
	v_mov_b32_e32 v76, v79
	v_pk_fma_f32 v[102:103], v[12:13], v[76:77], v[106:107] op_sel_hi:[1,0,1]
	s_waitcnt lgkmcnt(2)
	v_mov_b32_e32 v76, v83
	v_pk_fma_f32 v[106:107], v[12:13], v[80:81], v[110:111] op_sel:[0,1,0]
	v_pk_fma_f32 v[110:111], v[12:13], v[76:77], v[114:115] op_sel_hi:[1,0,1]
	s_waitcnt lgkmcnt(1)
	v_mov_b32_e32 v76, v87
	v_pk_fma_f32 v[92:93], v[12:13], v[76:77], v[92:93] op_sel_hi:[1,0,1]
	s_waitcnt lgkmcnt(0)
	v_mov_b32_e32 v76, v91
	v_pk_fma_f32 v[100:101], v[12:13], v[78:79], v[104:105] op_sel_hi:[1,0,1]
	v_pk_fma_f32 v[104:105], v[12:13], v[80:81], v[108:109] op_sel_hi:[1,0,1]
	v_pk_fma_f32 v[108:109], v[12:13], v[82:83], v[112:113] op_sel_hi:[1,0,1]
	v_pk_fma_f32 v[112:113], v[12:13], v[84:85], v[116:117] op_sel_hi:[1,0,1]
	v_pk_fma_f32 v[114:115], v[12:13], v[84:85], v[140:141] op_sel:[0,1,0]
	v_pk_fma_f32 v[116:117], v[12:13], v[86:87], v[142:143] op_sel_hi:[1,0,1]
	v_pk_fma_f32 v[140:141], v[12:13], v[88:89], v[144:145] op_sel_hi:[1,0,1]
	v_pk_fma_f32 v[94:95], v[12:13], v[88:89], v[94:95] op_sel:[0,1,0]
	v_pk_fma_f32 v[98:99], v[12:13], v[90:91], v[98:99] op_sel_hi:[1,0,1]
	v_pk_fma_f32 v[12:13], v[12:13], v[76:77], v[96:97] op_sel_hi:[1,0,1]
	ds_read_b128 v[76:79], v37 offset:15360
	ds_read_b128 v[80:83], v37 offset:15376
	ds_read_b128 v[84:87], v37 offset:15392
	ds_read_b128 v[88:91], v37 offset:15408
	v_mov_b32_e32 v96, v10
	v_mov_b32_e32 v97, v14
	s_waitcnt lgkmcnt(3)
	v_mov_b32_e32 v10, v79
	v_pk_fma_f32 v[102:103], v[96:97], v[10:11], v[102:103] op_sel_hi:[1,0,1]
	s_waitcnt lgkmcnt(2)
	v_mov_b32_e32 v10, v83
	v_pk_fma_f32 v[110:111], v[96:97], v[10:11], v[110:111] op_sel_hi:[1,0,1]
	s_waitcnt lgkmcnt(1)
	v_mov_b32_e32 v10, v87
	v_pk_fma_f32 v[92:93], v[96:97], v[10:11], v[92:93] op_sel_hi:[1,0,1]
	s_waitcnt lgkmcnt(0)
	v_mov_b32_e32 v10, v91
	v_pk_fma_f32 v[8:9], v[96:97], v[76:77], v[8:9] op_sel_hi:[1,0,1]
	v_pk_fma_f32 v[16:17], v[96:97], v[76:77], v[16:17] op_sel:[0,1,0]
	v_pk_fma_f32 v[12:13], v[96:97], v[10:11], v[12:13] op_sel_hi:[1,0,1]
	v_pk_fma_f32 v[100:101], v[96:97], v[78:79], v[100:101] op_sel_hi:[1,0,1]
	v_pk_fma_f32 v[104:105], v[96:97], v[80:81], v[104:105] op_sel_hi:[1,0,1]
	v_pk_fma_f32 v[106:107], v[96:97], v[80:81], v[106:107] op_sel:[0,1,0]
	v_pk_fma_f32 v[108:109], v[96:97], v[82:83], v[108:109] op_sel_hi:[1,0,1]
	v_pk_fma_f32 v[112:113], v[96:97], v[84:85], v[112:113] op_sel_hi:[1,0,1]
	v_pk_fma_f32 v[114:115], v[96:97], v[84:85], v[114:115] op_sel:[0,1,0]
	v_pk_fma_f32 v[116:117], v[96:97], v[86:87], v[116:117] op_sel_hi:[1,0,1]
	v_pk_fma_f32 v[140:141], v[96:97], v[88:89], v[140:141] op_sel_hi:[1,0,1]
	v_pk_fma_f32 v[94:95], v[96:97], v[88:89], v[94:95] op_sel:[0,1,0]
	v_pk_fma_f32 v[98:99], v[96:97], v[90:91], v[98:99] op_sel_hi:[1,0,1]
	ds_read_b128 v[76:79], v37 offset:35840
	ds_read_b128 v[80:83], v37 offset:35856
	ds_read_b128 v[84:87], v37 offset:35872
	ds_read_b128 v[88:91], v37 offset:35888
	v_mov_b32_e32 v14, v11
	s_waitcnt lgkmcnt(3)
	v_pk_fma_f32 v[96:97], v[14:15], v[76:77], v[8:9] op_sel_hi:[1,0,1]
	v_mov_b32_e32 v8, v79
	v_pk_fma_f32 v[102:103], v[14:15], v[8:9], v[102:103] op_sel_hi:[1,0,1]
	s_waitcnt lgkmcnt(2)
	v_mov_b32_e32 v8, v83
	v_pk_fma_f32 v[110:111], v[14:15], v[8:9], v[110:111] op_sel_hi:[1,0,1]
	s_waitcnt lgkmcnt(1)
	v_mov_b32_e32 v8, v87
	v_pk_fma_f32 v[112:113], v[14:15], v[84:85], v[112:113] op_sel_hi:[1,0,1]
	v_pk_fma_f32 v[84:85], v[14:15], v[84:85], v[114:115] op_sel:[0,1,0]
	v_pk_fma_f32 v[114:115], v[14:15], v[86:87], v[116:117] op_sel_hi:[1,0,1]
	v_pk_fma_f32 v[86:87], v[14:15], v[8:9], v[92:93] op_sel_hi:[1,0,1]
	s_waitcnt lgkmcnt(0)
	v_mov_b32_e32 v8, v91
	v_pk_fma_f32 v[16:17], v[14:15], v[76:77], v[16:17] op_sel:[0,1,0]
	v_pk_fma_f32 v[92:93], v[14:15], v[88:89], v[140:141] op_sel_hi:[1,0,1]
	v_pk_fma_f32 v[88:89], v[14:15], v[88:89], v[94:95] op_sel:[0,1,0]
	v_pk_fma_f32 v[94:95], v[14:15], v[90:91], v[98:99] op_sel_hi:[1,0,1]
	v_pk_fma_f32 v[90:91], v[14:15], v[8:9], v[12:13] op_sel_hi:[1,0,1]
	v_pk_fma_f32 v[100:101], v[14:15], v[78:79], v[100:101] op_sel_hi:[1,0,1]
	v_pk_fma_f32 v[104:105], v[14:15], v[80:81], v[104:105] op_sel_hi:[1,0,1]
	v_pk_fma_f32 v[106:107], v[14:15], v[80:81], v[106:107] op_sel:[0,1,0]
	v_pk_fma_f32 v[108:109], v[14:15], v[82:83], v[108:109] op_sel_hi:[1,0,1]
	ds_read_b128 v[8:11], v37 offset:56320
	ds_read_b128 v[12:15], v37 offset:56336
	ds_read_b128 v[76:79], v37 offset:56352
	ds_read_b128 v[80:83], v37 offset:56368
	v_mov_b32_e32 v98, v4
	v_mov_b32_e32 v99, v6
	s_waitcnt lgkmcnt(3)
	v_mov_b32_e32 v4, v11
	v_pk_fma_f32 v[102:103], v[98:99], v[4:5], v[102:103] op_sel_hi:[1,0,1]
	s_waitcnt lgkmcnt(2)
	v_mov_b32_e32 v4, v15
	v_pk_fma_f32 v[110:111], v[98:99], v[4:5], v[110:111] op_sel_hi:[1,0,1]
	s_waitcnt lgkmcnt(1)
	v_mov_b32_e32 v4, v79
	v_pk_fma_f32 v[16:17], v[98:99], v[8:9], v[16:17] op_sel:[0,1,0]
	v_pk_fma_f32 v[84:85], v[98:99], v[76:77], v[84:85] op_sel:[0,1,0]
	v_pk_fma_f32 v[140:141], v[98:99], v[4:5], v[86:87] op_sel_hi:[1,0,1]
	s_waitcnt lgkmcnt(0)
	v_mov_b32_e32 v4, v83
	v_pk_fma_f32 v[116:117], v[98:99], v[8:9], v[96:97] op_sel_hi:[1,0,1]
	v_pk_fma_f32 v[100:101], v[98:99], v[10:11], v[100:101] op_sel_hi:[1,0,1]
	v_pk_fma_f32 v[104:105], v[98:99], v[12:13], v[104:105] op_sel_hi:[1,0,1]
	v_pk_fma_f32 v[106:107], v[98:99], v[12:13], v[106:107] op_sel:[0,1,0]
	v_pk_fma_f32 v[108:109], v[98:99], v[14:15], v[108:109] op_sel_hi:[1,0,1]
	v_pk_fma_f32 v[112:113], v[98:99], v[76:77], v[112:113] op_sel_hi:[1,0,1]
	v_pk_fma_f32 v[114:115], v[98:99], v[78:79], v[114:115] op_sel_hi:[1,0,1]
	v_pk_fma_f32 v[142:143], v[98:99], v[80:81], v[92:93] op_sel_hi:[1,0,1]
	v_pk_fma_f32 v[144:145], v[98:99], v[80:81], v[88:89] op_sel:[0,1,0]
	v_pk_fma_f32 v[146:147], v[98:99], v[82:83], v[94:95] op_sel_hi:[1,0,1]
	v_pk_fma_f32 v[98:99], v[98:99], v[4:5], v[90:91] op_sel_hi:[1,0,1]
	v_add_u32_e32 v4, 0x12c00, v37
	v_add_u32_e32 v6, 0x12c10, v37
	ds_read_b128 v[8:11], v4
	ds_read_b128 v[80:83], v6
	v_add_u32_e32 v4, 0x12c20, v37
	v_add_u32_e32 v6, 0x12c30, v37
	ds_read_b128 v[88:91], v4
	ds_read_b128 v[94:97], v6
	v_mov_b32_e32 v6, v5
	s_waitcnt lgkmcnt(3)
	v_mov_b32_e32 v4, v11
	v_pk_fma_f32 v[76:77], v[6:7], v[4:5], v[102:103] op_sel_hi:[1,0,1]
	s_waitcnt lgkmcnt(2)
	v_pk_fma_f32 v[12:13], v[6:7], v[80:81], v[104:105] op_sel_hi:[1,0,1]
	v_pk_fma_f32 v[4:5], v[6:7], v[80:81], v[106:107] op_sel:[0,1,0]
	s_waitcnt lgkmcnt(1)
	v_mov_b32_e32 v80, v91
	v_pk_fma_f32 v[14:15], v[6:7], v[8:9], v[16:17] op_sel:[0,1,0]
	v_pk_fma_f32 v[16:17], v[6:7], v[10:11], v[100:101] op_sel_hi:[1,0,1]
	v_mov_b32_e32 v10, v83
	v_pk_fma_f32 v[92:93], v[6:7], v[88:89], v[112:113] op_sel_hi:[1,0,1]
	v_pk_fma_f32 v[86:87], v[6:7], v[88:89], v[84:85] op_sel:[0,1,0]
	v_pk_fma_f32 v[88:89], v[6:7], v[90:91], v[114:115] op_sel_hi:[1,0,1]
	v_pk_fma_f32 v[90:91], v[6:7], v[80:81], v[140:141] op_sel_hi:[1,0,1]
	s_waitcnt lgkmcnt(0)
	v_pk_fma_f32 v[84:85], v[6:7], v[94:95], v[142:143] op_sel_hi:[1,0,1]
	v_pk_fma_f32 v[80:81], v[6:7], v[94:95], v[144:145] op_sel:[0,1,0]
	v_mov_b32_e32 v94, v97
	v_pk_fma_f32 v[78:79], v[6:7], v[8:9], v[116:117] op_sel_hi:[1,0,1]
	v_pk_fma_f32 v[8:9], v[6:7], v[82:83], v[108:109] op_sel_hi:[1,0,1]
	v_pk_fma_f32 v[10:11], v[6:7], v[10:11], v[110:111] op_sel_hi:[1,0,1]
	v_pk_fma_f32 v[82:83], v[6:7], v[96:97], v[146:147] op_sel_hi:[1,0,1]
	v_pk_fma_f32 v[6:7], v[6:7], v[94:95], v[98:99] op_sel_hi:[1,0,1]
	s_nop 0
	s_nop 0
	s_nop 4
	v_permlane32_swap_b32_e32 v78, v92
	v_permlane32_swap_b32_e32 v14, v86
	v_permlane32_swap_b32_e32 v16, v88
	v_permlane32_swap_b32_e32 v76, v90
	v_permlane32_swap_b32_e32 v12, v84
	v_permlane32_swap_b32_e32 v4, v80
	v_permlane32_swap_b32_e32 v8, v82
	v_permlane32_swap_b32_e32 v10, v6
	v_add_f32_e32 v37, v92, v78
	v_add_f32_e32 v14, v86, v14
	v_add_f32_e32 v16, v88, v16
	v_add_f32_e32 v76, v90, v76
	v_add_f32_e32 v12, v84, v12
	v_add_f32_e32 v4, v80, v4
	v_add_f32_e32 v8, v82, v8
	v_add_f32_e32 v6, v6, v10
	s_nop 1
	v_permlane16_swap_b32_e32 v37, v12
	v_permlane16_swap_b32_e32 v14, v4
	v_permlane16_swap_b32_e32 v16, v8
	v_permlane16_swap_b32_e32 v76, v6
	v_add_f32_e32 v10, v12, v37
	v_add_f32_e32 v4, v4, v14
	v_add_f32_e32 v8, v8, v16
	v_add_f32_e32 v6, v6, v76
	v_cndmask_b32_e64 v12, v8, v10, s[10:11]
	v_cndmask_b32_e64 v8, v10, v8, s[10:11]
	v_cndmask_b32_e64 v10, v6, v4, s[10:11]
	v_cndmask_b32_e64 v4, v4, v6, s[10:11]
	s_nop 1
	v_add_f32_dpp v8, v8, v12 row_ror:8 row_mask:0xf bank_mask:0xf
	v_add_f32_dpp v4, v4, v10 row_ror:8 row_mask:0xf bank_mask:0xf
	v_cndmask_b32_e64 v6, v4, v8, s[12:13]
	v_cndmask_b32_e64 v4, v8, v4, s[12:13]
	s_nop 1
	v_add_f32_dpp v164, v4, v6 row_shl:4 row_mask:0xf bank_mask:0x5
	v_add_f32_dpp v164, v4, v6 row_shr:4 row_mask:0xf bank_mask:0xa
	s_nop 1
	v_add_f32_dpp v165, v164, v164 quad_perm:[2,3,0,1] row_mask:0xf bank_mask:0xf
	s_nop 1
	v_add_f32_dpp v4, v165, v165 quad_perm:[1,0,3,2] row_mask:0xf bank_mask:0xf
	v_mov_b32_e32 v164, v4
	v_mov_b32_e32 v165, v4
	s_nop 1
	v_permlane32_swap_b32_e32 v164, v165
	v_max_f32_e32 v6, v164, v165
	v_mov_b32_e32 v164, v6
	v_mov_b32_e32 v165, v6
	s_nop 1
	v_permlane16_swap_b32_e32 v164, v165
	v_max_f32_e32 v6, v164, v165
	s_nop 1
	v_max_f32_dpp v6, v6, v6 row_ror:8 row_mask:0xf bank_mask:0xf
	s_nop 1
	v_max_f32_dpp v6, v6, v6 row_half_mirror row_mask:0xf bank_mask:0xf
	v_sub_f32_e32 v4, v4, v6
	v_mul_f32_e32 v6, 0x3fb8aa3b, v4
	v_fma_f32 v8, v4, s33, -v6
	v_rndne_f32_e32 v10, v6
	v_fmac_f32_e32 v8, 0x32a5705f, v4
	v_sub_f32_e32 v6, v6, v10
	v_add_f32_e32 v6, v6, v8
	v_exp_f32_e32 v6, v6
	v_cvt_i32_f32_e32 v8, v10
	v_cmp_ngt_f32_e32 vcc, s36, v4
	v_ldexp_f32 v6, v6, v8
	s_nop 0
	v_cndmask_b32_e32 v6, 0, v6, vcc
	v_cmp_nlt_f32_e32 vcc, s53, v4
	s_nop 1
	v_cndmask_b32_e32 v4, v216, v6, vcc
	v_mov_b32_e32 v164, v4
	v_mov_b32_e32 v165, v4
	s_nop 1
	v_permlane32_swap_b32_e32 v164, v165
	v_add_f32_e32 v6, v164, v165
	v_mov_b32_e32 v164, v6
	v_mov_b32_e32 v165, v6
	s_nop 1
	v_permlane16_swap_b32_e32 v164, v165
	v_add_f32_e32 v6, v164, v165
	s_nop 1
	v_add_f32_dpp v6, v6, v6 row_ror:8 row_mask:0xf bank_mask:0xf
	s_nop 1
	v_add_f32_dpp v6, v6, v6 row_half_mirror row_mask:0xf bank_mask:0xf
	s_and_saveexec_b64 s[16:17], s[14:15]
	s_cbranch_execz .LBB0_1263
	v_div_scale_f32 v8, s[34:35], v6, v6, v4
	v_rcp_f32_e32 v10, v8
	v_div_scale_f32 v12, vcc, v4, v6, v4
	v_lshl_add_u64 v[94:95], s[62:63], 0, v[38:39]
	v_fma_f32 v14, -v8, v10, 1.0
	v_fmac_f32_e32 v10, v14, v10
	v_mul_f32_e32 v14, v12, v10
	v_fma_f32 v16, -v8, v14, v12
	v_fmac_f32_e32 v14, v16, v10
	v_fma_f32 v8, -v8, v14, v12
	v_div_fmas_f32 v8, v8, v10, v14
	v_div_fixup_f32 v4, v8, v6, v4
	global_store_dword v[94:95], v4, off

.LBB0_1265:
	s_cmp_eq_u32 s100, 1
	s_cbranch_scc1 .Lmy_n2_ret
	s_mov_b64 s[6:7], s[96:97]
	s_getreg_b32 s1, hwreg(HW_REG_XCC_ID, 0, 4)
	s_waitcnt vmcnt(0)
	s_waitcnt lgkmcnt(0)
	s_barrier
	s_and_saveexec_b64 s[4:5], s[20:21]
	s_cbranch_execz .LBB0_1317
	v_readlane_b32 s2, v254, 22
	s_load_dwordx2 s[6:7], s[6:7], 0xe0
	s_waitcnt vmcnt(0) expcnt(0) lgkmcnt(0)
	v_mov_b32_e32 v2, s2
	ds_read_b32 v4, v2
	v_readlane_b32 s2, v254, 23
	s_and_b32 s1, s1, 15
	s_waitcnt lgkmcnt(0)
	v_cmp_ne_u32_e32 vcc, 0, v4
	v_mov_b32_e32 v2, s2
	ds_read_b32 v2, v2
	s_cbranch_vccnz .LBB0_1281
	v_readlane_b32 s8, v254, 3
	v_readlane_b32 s9, v254, 4
	s_load_dwordx2 s[12:13], s[8:9], 0x4
	s_add_u32 s8, s6, 0x1000
	s_addc_u32 s9, s7, 0
	s_add_u32 s10, s6, 0x1100
	s_addc_u32 s11, s7, 0
	v_readlane_b32 s2, v254, 0
	s_waitcnt lgkmcnt(0)
	s_mul_i32 s2, s12, s2
	s_add_u32 s12, s6, 0x1200
	s_mul_i32 s2, s2, s13
	s_addc_u32 s13, s7, 0
	s_add_u32 s14, s6, 0x1300
	s_addc_u32 s15, s7, 0
	s_mov_b32 s22, 1
	s_branch .LBB0_1269
